# same as v63 except the converter workgroup count is derived from gridDim (grid-192) instead of the constant 64; identical behaviour at 256 workgroups
# baseline (speedup 1.0000x reference)
.LBB0_400:
	s_cmp_lt_i32 s76, 2
	s_cselect_b64 s[6:7], -1, 0
	s_add_u32 s82, s58, 0x32100000
	s_addc_u32 s83, s59, 0
	s_and_b64 s[0:1], s[6:7], s[0:1]
	s_andn2_b64 vcc, exec, s[0:1]
	s_cbranch_vccnz .LBB0_417
	s_mov_b32 s101, s2
	s_cmpk_lt_i32 s96, 192
	s_cbranch_scc1 .Lh0_gemm
	s_sub_i32 s96, s96, 192
	s_sub_i32 s2, s101, 192
	s_mov_b32 s98, 2
	s_mov_b32 s100, 5
	s_mov_b32 s99, 1
	v_readlane_b32 s6, v239, 34
	v_readlane_b32 s7, v239, 35
	s_nop 3
	s_sub_u32 s6, s6, 0x128
	s_subb_u32 s7, s7, 0
	s_load_dwordx2 s[82:83], s[6:7], 0xc8
	s_waitcnt lgkmcnt(0)
	s_branch .Lconv_entry
